# baseline (speedup 1.0000x reference)
.LBB1_116:
	s_or_b64 exec, exec, s[14:15]
	v_mov_b32_e32 v50, v0
	s_lshr_b32 s0, s34, 13
	v_and_b32_e32 v52, 15, v50
	s_waitcnt lgkmcnt(0)
	v_lshlrev_b32_e32 v55, 2, v50
	v_lshlrev_b32_e32 v52, 6, v52
	v_and_b32_e32 v53, 48, v50
	v_lshlrev_b32_e32 v54, 6, v50
	v_and_b32_e32 v55, 32, v55
	v_bitop3_b32 v237, v52, v55, v53 bitop3:0x36
	v_and_b32_e32 v52, 0x3c0, v54
	v_lshlrev_b32_e32 v56, 7, v50
	v_bitop3_b32 v52, v52, v55, v53 bitop3:0x36
	v_and_or_b32 v238, v56, s23, v52
	v_lshlrev_b32_e32 v52, 8, v50
	v_lshlrev_b32_e32 v53, 3, v50
	v_lshlrev_b32_e32 v50, 4, v50
	v_and_b32_e32 v52, 0x400, v52
	v_and_b32_e32 v55, 0x1c0, v53
	v_and_b32_e32 v50, 48, v50
	s_and_b32 s0, s0, 0x3800
	v_or3_b32 v50, v52, v50, v55
	v_and_b32_e32 v52, 0xfffff000, v54
	s_bfe_u32 s17, s34, 0x80010
	s_mulk_i32 s0, 0xc00
	v_or_b32_e32 v239, v50, v52
	v_bitop3_b32 v240, v50, s30, v52 bitop3:0x36
	v_and_or_b32 v50, v53, s26, v52
	s_add_u32 s0, s4, s0
	v_add_u32_e32 v241, 0x8000, v50
	v_add_u32_e32 v50, 0x8200, v50
	s_addc_u32 s1, s5, 0
	s_lshl_b32 s35, s17, 7
	v_xor_b32_e32 v242, 32, v50
	s_cmp_lt_u32 s34, 0x8000000
	v_mov_b32_e32 v50, 0x24000
	v_mov_b32_e32 v170, 0
	v_and_b32_e32 v236, 0x4000, v54
	v_lshl_add_u32 v243, v51, 10, v50
	s_cselect_b32 s1, s1, s7
	s_cselect_b32 s0, s0, s6
	s_mov_b32 s36, 0
	s_xor_b64 s[2:3], s[12:13], -1
	v_mov_b32_e32 v234, v228
	s_mov_b32 s16, s21
	s_mov_b32 s37, 0
	v_mov_b32_e32 v171, v170
	v_mov_b32_e32 v172, v170
	v_mov_b32_e32 v173, v170
	v_mov_b32_e32 v162, v170
	v_mov_b32_e32 v163, v170
	v_mov_b32_e32 v164, v170
	v_mov_b32_e32 v165, v170
	v_mov_b32_e32 v174, v170
	v_mov_b32_e32 v175, v170
	v_mov_b32_e32 v176, v170
	v_mov_b32_e32 v177, v170
	v_mov_b32_e32 v166, v170
	v_mov_b32_e32 v167, v170
	v_mov_b32_e32 v168, v170
	v_mov_b32_e32 v169, v170
	v_mov_b32_e32 v154, v170
	v_mov_b32_e32 v155, v170
	v_mov_b32_e32 v156, v170
	v_mov_b32_e32 v157, v170
	v_mov_b32_e32 v146, v170
	v_mov_b32_e32 v147, v170
	v_mov_b32_e32 v148, v170
	v_mov_b32_e32 v149, v170
	v_mov_b32_e32 v158, v170
	v_mov_b32_e32 v159, v170
	v_mov_b32_e32 v160, v170
	v_mov_b32_e32 v161, v170
	v_mov_b32_e32 v150, v170
	v_mov_b32_e32 v151, v170
	v_mov_b32_e32 v152, v170
	v_mov_b32_e32 v153, v170
	v_mov_b32_e32 v138, v170
	v_mov_b32_e32 v139, v170
	v_mov_b32_e32 v140, v170
	v_mov_b32_e32 v141, v170
	v_mov_b32_e32 v130, v170
	v_mov_b32_e32 v131, v170
	v_mov_b32_e32 v132, v170
	v_mov_b32_e32 v133, v170
	v_mov_b32_e32 v142, v170
	v_mov_b32_e32 v143, v170
	v_mov_b32_e32 v144, v170
	v_mov_b32_e32 v145, v170
	v_mov_b32_e32 v134, v170
	v_mov_b32_e32 v135, v170
	v_mov_b32_e32 v136, v170
	v_mov_b32_e32 v137, v170
	v_mov_b32_e32 v122, v170
	v_mov_b32_e32 v123, v170
	v_mov_b32_e32 v124, v170
	v_mov_b32_e32 v125, v170
	v_mov_b32_e32 v114, v170
	v_mov_b32_e32 v115, v170
	v_mov_b32_e32 v116, v170
	v_mov_b32_e32 v117, v170
	v_mov_b32_e32 v126, v170
	v_mov_b32_e32 v127, v170
	v_mov_b32_e32 v128, v170
	v_mov_b32_e32 v129, v170
	v_mov_b32_e32 v118, v170
	v_mov_b32_e32 v119, v170
	v_mov_b32_e32 v120, v170
	v_mov_b32_e32 v121, v170
	v_mov_b32_e32 v106, v170
	v_mov_b32_e32 v107, v170
	v_mov_b32_e32 v108, v170
	v_mov_b32_e32 v109, v170
	v_mov_b32_e32 v98, v170
	v_mov_b32_e32 v99, v170
	v_mov_b32_e32 v100, v170
	v_mov_b32_e32 v101, v170
	v_mov_b32_e32 v110, v170
	v_mov_b32_e32 v111, v170
	v_mov_b32_e32 v112, v170
	v_mov_b32_e32 v113, v170
	v_mov_b32_e32 v102, v170
	v_mov_b32_e32 v103, v170
	v_mov_b32_e32 v104, v170
	v_mov_b32_e32 v105, v170
	v_mov_b32_e32 v90, v170
	v_mov_b32_e32 v91, v170
	v_mov_b32_e32 v92, v170
	v_mov_b32_e32 v93, v170
	v_mov_b32_e32 v82, v170
	v_mov_b32_e32 v83, v170
	v_mov_b32_e32 v84, v170
	v_mov_b32_e32 v85, v170
	v_mov_b32_e32 v94, v170
	v_mov_b32_e32 v95, v170
	v_mov_b32_e32 v96, v170
	v_mov_b32_e32 v97, v170
	v_mov_b32_e32 v86, v170
	v_mov_b32_e32 v87, v170
	v_mov_b32_e32 v88, v170
	v_mov_b32_e32 v89, v170
	v_mov_b32_e32 v74, v170
	v_mov_b32_e32 v75, v170
	v_mov_b32_e32 v76, v170
	v_mov_b32_e32 v77, v170
	v_mov_b32_e32 v66, v170
	v_mov_b32_e32 v67, v170
	v_mov_b32_e32 v68, v170
	v_mov_b32_e32 v69, v170
	v_mov_b32_e32 v78, v170
	v_mov_b32_e32 v79, v170
	v_mov_b32_e32 v80, v170
	v_mov_b32_e32 v81, v170
	v_mov_b32_e32 v70, v170
	v_mov_b32_e32 v71, v170
	v_mov_b32_e32 v72, v170
	v_mov_b32_e32 v73, v170
	v_mov_b32_e32 v62, v170
	v_mov_b32_e32 v63, v170
	v_mov_b32_e32 v64, v170
	v_mov_b32_e32 v65, v170
	v_mov_b32_e32 v54, v170
	v_mov_b32_e32 v55, v170
	v_mov_b32_e32 v56, v170
	v_mov_b32_e32 v57, v170
	v_mov_b32_e32 v58, v170
	v_mov_b32_e32 v59, v170
	v_mov_b32_e32 v60, v170
	v_mov_b32_e32 v61, v170
	v_mov_b32_e32 v50, v170
	v_mov_b32_e32 v51, v170
	v_mov_b32_e32 v52, v170
	v_mov_b32_e32 v53, v170
	s_branch .LBB1_118
	s_nop 0
	s_nop 0
	s_nop 0
	s_nop 0
